# baseline (speedup 1.0000x reference)
.Lg0_cloop:
	s_mul_i32 s8, s3, 0x7000
	s_barrier
	v_add_u32_e32 v103, s8, v100
	v_add_u32_e32 v101, s8, v99
	ds_read_b128 v[146:149], v103 offset:12288
	ds_read_b128 v[150:153], v103 offset:13312
	ds_read_b128 v[154:157], v103 offset:14336
	ds_read_b128 v[158:161], v103 offset:15360
	s_waitcnt lgkmcnt(9)
	v_mfma_f32_16x16x32_f16 v[94:97], v[122:125], v[104:107], v[94:97]
	s_add_i32 s8, s3, 1
	s_cmp_lg_u32 s3, 4
	s_cselect_b32 s3, s8, 0
	v_mfma_f32_16x16x32_f16 v[70:73], v[122:125], v[108:111], v[70:73]
	v_mfma_f32_16x16x32_f16 v[46:49], v[122:125], v[112:115], v[46:49]
	v_mfma_f32_16x16x32_f16 v[22:25], v[122:125], v[116:119], v[22:25]
	ds_read_b128 v[122:125], v101
	s_waitcnt lgkmcnt(9)
	v_mfma_f32_16x16x32_f16 v[90:93], v[126:129], v[104:107], v[90:93]
	v_mfma_f32_16x16x32_f16 v[66:69], v[126:129], v[108:111], v[66:69]
	v_mfma_f32_16x16x32_f16 v[42:45], v[126:129], v[112:115], v[42:45]
	v_mfma_f32_16x16x32_f16 v[18:21], v[126:129], v[116:119], v[18:21]
	ds_read_b128 v[126:129], v101 offset:1024
	s_waitcnt lgkmcnt(9)
	v_mfma_f32_16x16x32_f16 v[86:89], v[130:133], v[104:107], v[86:89]
	v_mfma_f32_16x16x32_f16 v[54:57], v[130:133], v[108:111], v[54:57]
	v_mfma_f32_16x16x32_f16 v[26:29], v[130:133], v[112:115], v[26:29]
	v_mfma_f32_16x16x32_f16 v[6:9], v[130:133], v[116:119], v[6:9]
	ds_read_b128 v[130:133], v101 offset:2048
	s_waitcnt lgkmcnt(9)
	v_mfma_f32_16x16x32_f16 v[74:77], v[134:137], v[104:107], v[74:77]
	v_mfma_f32_16x16x32_f16 v[50:53], v[134:137], v[108:111], v[50:53]
	v_mfma_f32_16x16x32_f16 v[38:41], v[134:137], v[112:115], v[38:41]
	v_mfma_f32_16x16x32_f16 v[14:17], v[134:137], v[116:119], v[14:17]
	ds_read_b128 v[134:137], v101 offset:3072
	s_waitcnt lgkmcnt(9)
	v_mfma_f32_16x16x32_f16 v[82:85], v[138:141], v[104:107], v[82:85]
	v_mfma_f32_16x16x32_f16 v[58:61], v[138:141], v[108:111], v[58:61]
	v_mfma_f32_16x16x32_f16 v[30:33], v[138:141], v[112:115], v[30:33]
	v_mfma_f32_16x16x32_f16 v[10:13], v[138:141], v[116:119], v[10:13]
	ds_read_b128 v[138:141], v101 offset:4096
	s_waitcnt lgkmcnt(9)
	v_mfma_f32_16x16x32_f16 v[78:81], v[142:145], v[104:107], v[78:81]
	v_mfma_f32_16x16x32_f16 v[62:65], v[142:145], v[108:111], v[62:65]
	v_mfma_f32_16x16x32_f16 v[34:37], v[142:145], v[112:115], v[34:37]
	v_mfma_f32_16x16x32_f16 v[2:5], v[142:145], v[116:119], v[2:5]
	ds_read_b128 v[142:145], v101 offset:5120
	s_mul_i32 s8, s3, 0x7000
	s_barrier
	v_add_u32_e32 v103, s8, v100
	v_add_u32_e32 v101, s8, v99
	ds_read_b128 v[104:107], v103 offset:12288
	ds_read_b128 v[108:111], v103 offset:13312
	ds_read_b128 v[112:115], v103 offset:14336
	ds_read_b128 v[116:119], v103 offset:15360
	s_waitcnt lgkmcnt(9)
	v_mfma_f32_16x16x32_f16 v[94:97], v[122:125], v[146:149], v[94:97]
	s_add_i32 s8, s3, 1
	s_cmp_lg_u32 s3, 4
	s_cselect_b32 s3, s8, 0
	v_mfma_f32_16x16x32_f16 v[70:73], v[122:125], v[150:153], v[70:73]
	v_mfma_f32_16x16x32_f16 v[46:49], v[122:125], v[154:157], v[46:49]
	v_mfma_f32_16x16x32_f16 v[22:25], v[122:125], v[158:161], v[22:25]
	ds_read_b128 v[122:125], v101
	s_waitcnt lgkmcnt(9)
	v_mfma_f32_16x16x32_f16 v[90:93], v[126:129], v[146:149], v[90:93]
	v_mfma_f32_16x16x32_f16 v[66:69], v[126:129], v[150:153], v[66:69]
	v_mfma_f32_16x16x32_f16 v[42:45], v[126:129], v[154:157], v[42:45]
	v_mfma_f32_16x16x32_f16 v[18:21], v[126:129], v[158:161], v[18:21]
	ds_read_b128 v[126:129], v101 offset:1024
	s_waitcnt lgkmcnt(9)
	v_mfma_f32_16x16x32_f16 v[86:89], v[130:133], v[146:149], v[86:89]
	v_mfma_f32_16x16x32_f16 v[54:57], v[130:133], v[150:153], v[54:57]
	v_mfma_f32_16x16x32_f16 v[26:29], v[130:133], v[154:157], v[26:29]
	v_mfma_f32_16x16x32_f16 v[6:9], v[130:133], v[158:161], v[6:9]
	ds_read_b128 v[130:133], v101 offset:2048
	s_waitcnt lgkmcnt(9)
	v_mfma_f32_16x16x32_f16 v[74:77], v[134:137], v[146:149], v[74:77]
	v_mfma_f32_16x16x32_f16 v[50:53], v[134:137], v[150:153], v[50:53]
	v_mfma_f32_16x16x32_f16 v[38:41], v[134:137], v[154:157], v[38:41]
	v_mfma_f32_16x16x32_f16 v[14:17], v[134:137], v[158:161], v[14:17]
	ds_read_b128 v[134:137], v101 offset:3072
	s_waitcnt lgkmcnt(9)
	v_mfma_f32_16x16x32_f16 v[82:85], v[138:141], v[146:149], v[82:85]
	v_mfma_f32_16x16x32_f16 v[58:61], v[138:141], v[150:153], v[58:61]
	v_mfma_f32_16x16x32_f16 v[30:33], v[138:141], v[154:157], v[30:33]
	v_mfma_f32_16x16x32_f16 v[10:13], v[138:141], v[158:161], v[10:13]
	ds_read_b128 v[138:141], v101 offset:4096
	s_waitcnt lgkmcnt(9)
	v_mfma_f32_16x16x32_f16 v[78:81], v[142:145], v[146:149], v[78:81]
	v_mfma_f32_16x16x32_f16 v[62:65], v[142:145], v[150:153], v[62:65]
	v_mfma_f32_16x16x32_f16 v[34:37], v[142:145], v[154:157], v[34:37]
	v_mfma_f32_16x16x32_f16 v[2:5], v[142:145], v[158:161], v[2:5]
	ds_read_b128 v[142:145], v101 offset:5120
	s_add_i32 s7, s7, -1
	s_cmp_eq_u32 s7, 0
	s_cbranch_scc0 .Lg0_cloop
	s_waitcnt lgkmcnt(0)
	s_mul_i32 s24, s22, 0x3400
	s_lshl_b32 s28, s2, 6
	s_add_i32 s29, s20, s28
	s_and_b32 s30, s29, 0x7ff
	v_add_u32_e32 v98, s30, v102
	v_lshlrev_b32_e32 v98, 8, v98
	v_lshl_add_u32 v98, v120, 4, v98
	v_add_u32_e32 v99, 0x1000, v98
	v_add_u32_e32 v100, 0x2000, v98
	v_add_u32_e32 v101, 0x3000, v98
	v_mul_u32_u24_e32 v103, 0xd0, v102
	v_lshl_add_u32 v103, v120, 3, v103
	v_add_u32_e32 v103, s24, v103
	v_lshrrev_b32_e32 v0, 2, v1
	v_and_b32_e32 v1, 3, v1
	v_mul_u32_u24_e32 v102, 0xd0, v0
	v_lshl_add_u32 v102, v1, 4, v102
	v_add_u32_e32 v102, s24, v102
	v_lshlrev_b32_e32 v0, 11, v0
	v_lshl_add_u32 v0, v1, 4, v0
	s_lshl_b32 s31, s5, 7
	s_add_i32 s35, s31, 0
	s_and_b32 s35, s35, 0xff
	s_add_u32 s36, s12, s35
	s_addc_u32 s37, s13, 0
	s_add_i32 s35, s31, 64
	s_and_b32 s35, s35, 0xff
	s_add_u32 s38, s12, s35
	s_addc_u32 s39, s13, 0
	s_add_i32 s35, s31, 128
	s_and_b32 s35, s35, 0xff
	s_add_u32 s40, s12, s35
	s_addc_u32 s41, s13, 0
	s_add_i32 s35, s31, 192
	s_and_b32 s35, s35, 0xff
	s_add_u32 s42, s12, s35
	s_addc_u32 s43, s13, 0
	s_add_i32 s34, s25, s23
	s_sub_i32 s32, 0x400, s34
	s_ashr_i32 s32, s32, 4
	s_max_i32 s32, s32, 0
	s_min_i32 s32, s32, 6
	s_sub_i32 s33, 0x800, s34
	s_ashr_i32 s33, s33, 4
	s_max_i32 s33, s33, 0
	s_min_i32 s33, s33, 6
	s_cmp_eq_u32 s33, 0
	s_cbranch_scc1 .Lepi_noload
	s_cmp_lg_u32 s5, 0
	s_cbranch_scc1 .Lepi_ldw1
	global_load_dwordx4 v[108:111], v98, s[38:39]
	global_load_dwordx4 v[124:127], v99, s[38:39]
	global_load_dwordx4 v[140:143], v100, s[38:39]
	global_load_dwordx4 v[156:159], v101, s[38:39]
	global_load_dwordx4 v[104:107], v98, s[36:37]
	global_load_dwordx4 v[120:123], v99, s[36:37]
	global_load_dwordx4 v[136:139], v100, s[36:37]
	global_load_dwordx4 v[152:155], v101, s[36:37]
	global_load_dwordx4 v[116:119], v98, s[42:43]
	global_load_dwordx4 v[132:135], v99, s[42:43]
	global_load_dwordx4 v[148:151], v100, s[42:43]
	global_load_dwordx4 v[164:167], v101, s[42:43]
	global_load_dwordx4 v[112:115], v98, s[40:41]
	global_load_dwordx4 v[128:131], v99, s[40:41]
	global_load_dwordx4 v[144:147], v100, s[40:41]
	global_load_dwordx4 v[160:163], v101, s[40:41]
	s_branch .Lepi_noload
.Lepi_ldw1:
	global_load_dwordx4 v[116:119], v98, s[42:43]
	global_load_dwordx4 v[132:135], v99, s[42:43]
	global_load_dwordx4 v[148:151], v100, s[42:43]
	global_load_dwordx4 v[164:167], v101, s[42:43]
	global_load_dwordx4 v[112:115], v98, s[40:41]
	global_load_dwordx4 v[128:131], v99, s[40:41]
	global_load_dwordx4 v[144:147], v100, s[40:41]
	global_load_dwordx4 v[160:163], v101, s[40:41]
	global_load_dwordx4 v[108:111], v98, s[38:39]
	global_load_dwordx4 v[124:127], v99, s[38:39]
	global_load_dwordx4 v[140:143], v100, s[38:39]
	global_load_dwordx4 v[156:159], v101, s[38:39]
	global_load_dwordx4 v[104:107], v98, s[36:37]
	global_load_dwordx4 v[120:123], v99, s[36:37]
	global_load_dwordx4 v[136:139], v100, s[36:37]
	global_load_dwordx4 v[152:155], v101, s[36:37]
.Lepi_noload:
	s_barrier
	s_cmp_lg_u32 s5, 0
	s_cbranch_scc1 .Lepi_w1
	s_cmp_le_u32 s33, 5
	s_cbranch_scc1 .Lepi_v5
	s_waitcnt vmcnt(12)
	s_cmp_le_u32 s32, 5
	s_cbranch_scc1 .Lepi_r5
	v_mul_f32_e32 v108, 0x3e38aa3b, v108
	v_mul_f32_e32 v109, 0x3e38aa3b, v109
	v_mul_f32_e32 v110, 0x3e38aa3b, v110
	v_mul_f32_e32 v111, 0x3e38aa3b, v111
	v_mul_f32_e32 v124, 0x3e38aa3b, v124
	v_mul_f32_e32 v125, 0x3e38aa3b, v125
	v_mul_f32_e32 v126, 0x3e38aa3b, v126
	v_mul_f32_e32 v127, 0x3e38aa3b, v127
	v_mul_f32_e32 v140, 0x3e38aa3b, v140
	v_mul_f32_e32 v141, 0x3e38aa3b, v141
	v_mul_f32_e32 v142, 0x3e38aa3b, v142
	v_mul_f32_e32 v143, 0x3e38aa3b, v143
	v_mul_f32_e32 v156, 0x3e38aa3b, v156
	v_mul_f32_e32 v157, 0x3e38aa3b, v157
	v_mul_f32_e32 v158, 0x3e38aa3b, v158
	v_mul_f32_e32 v159, 0x3e38aa3b, v159

.Lepi_v0:
	v_cvt_pk_f16_f32 v94, v94, v95
	v_cvt_pk_f16_f32 v95, v96, v97
	ds_write_b64 v103, v[94:95] offset:0
	v_cvt_pk_f16_f32 v70, v70, v71
	v_cvt_pk_f16_f32 v71, v72, v73
	ds_write_b64 v103, v[70:71] offset:3328
	v_cvt_pk_f16_f32 v46, v46, v47
	v_cvt_pk_f16_f32 v47, v48, v49
	ds_write_b64 v103, v[46:47] offset:6656
	v_cvt_pk_f16_f32 v22, v22, v23
	v_cvt_pk_f16_f32 v23, v24, v25
	ds_write_b64 v103, v[22:23] offset:9984
.Lepi_d0:
	s_branch .Lepi_join
.Lepi_w1:
	s_cmp_le_u32 s33, 3
	s_cbranch_scc1 .Lepi_v3w
	s_waitcnt vmcnt(12)
	s_cmp_le_u32 s32, 3
	s_cbranch_scc1 .Lepi_r3w
	v_mul_f32_e32 v116, 0x3e38aa3b, v116
	v_mul_f32_e32 v117, 0x3e38aa3b, v117
	v_mul_f32_e32 v118, 0x3e38aa3b, v118
	v_mul_f32_e32 v119, 0x3e38aa3b, v119
	v_mul_f32_e32 v132, 0x3e38aa3b, v132
	v_mul_f32_e32 v133, 0x3e38aa3b, v133
	v_mul_f32_e32 v134, 0x3e38aa3b, v134
	v_mul_f32_e32 v135, 0x3e38aa3b, v135
	v_mul_f32_e32 v148, 0x3e38aa3b, v148
	v_mul_f32_e32 v149, 0x3e38aa3b, v149
	v_mul_f32_e32 v150, 0x3e38aa3b, v150
	v_mul_f32_e32 v151, 0x3e38aa3b, v151
	v_mul_f32_e32 v164, 0x3e38aa3b, v164
	v_mul_f32_e32 v165, 0x3e38aa3b, v165
	v_mul_f32_e32 v166, 0x3e38aa3b, v166
	v_mul_f32_e32 v167, 0x3e38aa3b, v167

.Lepi_d3w:
	s_cmp_le_u32 s33, 2
	s_cbranch_scc1 .Lepi_v2w
	s_waitcnt vmcnt(8)
	s_cmp_le_u32 s32, 2
	s_cbranch_scc1 .Lepi_r2w
	v_mul_f32_e32 v112, 0x3e38aa3b, v112
	v_mul_f32_e32 v113, 0x3e38aa3b, v113
	v_mul_f32_e32 v114, 0x3e38aa3b, v114
	v_mul_f32_e32 v115, 0x3e38aa3b, v115
	v_mul_f32_e32 v128, 0x3e38aa3b, v128
	v_mul_f32_e32 v129, 0x3e38aa3b, v129
	v_mul_f32_e32 v130, 0x3e38aa3b, v130
	v_mul_f32_e32 v131, 0x3e38aa3b, v131
	v_mul_f32_e32 v144, 0x3e38aa3b, v144
	v_mul_f32_e32 v145, 0x3e38aa3b, v145
	v_mul_f32_e32 v146, 0x3e38aa3b, v146
	v_mul_f32_e32 v147, 0x3e38aa3b, v147
	v_mul_f32_e32 v160, 0x3e38aa3b, v160
	v_mul_f32_e32 v161, 0x3e38aa3b, v161
	v_mul_f32_e32 v162, 0x3e38aa3b, v162
	v_mul_f32_e32 v163, 0x3e38aa3b, v163

.Lepi_d2w:
	s_cmp_le_u32 s33, 5
	s_cbranch_scc1 .Lepi_v5w
	s_waitcnt vmcnt(4)
	s_cmp_le_u32 s32, 5
	s_cbranch_scc1 .Lepi_r5w
	v_mul_f32_e32 v108, 0x3e38aa3b, v108
	v_mul_f32_e32 v109, 0x3e38aa3b, v109
	v_mul_f32_e32 v110, 0x3e38aa3b, v110
	v_mul_f32_e32 v111, 0x3e38aa3b, v111
	v_mul_f32_e32 v124, 0x3e38aa3b, v124
	v_mul_f32_e32 v125, 0x3e38aa3b, v125
	v_mul_f32_e32 v126, 0x3e38aa3b, v126
	v_mul_f32_e32 v127, 0x3e38aa3b, v127
	v_mul_f32_e32 v140, 0x3e38aa3b, v140
	v_mul_f32_e32 v141, 0x3e38aa3b, v141
	v_mul_f32_e32 v142, 0x3e38aa3b, v142
	v_mul_f32_e32 v143, 0x3e38aa3b, v143
	v_mul_f32_e32 v156, 0x3e38aa3b, v156
	v_mul_f32_e32 v157, 0x3e38aa3b, v157
	v_mul_f32_e32 v158, 0x3e38aa3b, v158
	v_mul_f32_e32 v159, 0x3e38aa3b, v159

.Lepi_d5w:
	s_cmp_le_u32 s33, 4
	s_cbranch_scc1 .Lepi_v4w
	s_waitcnt vmcnt(0)
	s_cmp_le_u32 s32, 4
	s_cbranch_scc1 .Lepi_r4w
	v_mul_f32_e32 v104, 0x3e38aa3b, v104
	v_mul_f32_e32 v105, 0x3e38aa3b, v105
	v_mul_f32_e32 v106, 0x3e38aa3b, v106
	v_mul_f32_e32 v107, 0x3e38aa3b, v107
	v_mul_f32_e32 v120, 0x3e38aa3b, v120
	v_mul_f32_e32 v121, 0x3e38aa3b, v121
	v_mul_f32_e32 v122, 0x3e38aa3b, v122
	v_mul_f32_e32 v123, 0x3e38aa3b, v123
	v_mul_f32_e32 v136, 0x3e38aa3b, v136
	v_mul_f32_e32 v137, 0x3e38aa3b, v137
	v_mul_f32_e32 v138, 0x3e38aa3b, v138
	v_mul_f32_e32 v139, 0x3e38aa3b, v139
	v_mul_f32_e32 v152, 0x3e38aa3b, v152
	v_mul_f32_e32 v153, 0x3e38aa3b, v153
	v_mul_f32_e32 v154, 0x3e38aa3b, v154
	v_mul_f32_e32 v155, 0x3e38aa3b, v155

.Lepi_v4w:
	v_cvt_pk_f16_f32 v82, v82, v83
	v_cvt_pk_f16_f32 v83, v84, v85
	ds_write_b64 v103, v[82:83] offset:128
	v_cvt_pk_f16_f32 v58, v58, v59
	v_cvt_pk_f16_f32 v59, v60, v61
	ds_write_b64 v103, v[58:59] offset:3456
	v_cvt_pk_f16_f32 v30, v30, v31
	v_cvt_pk_f16_f32 v31, v32, v33
	ds_write_b64 v103, v[30:31] offset:6784
	v_cvt_pk_f16_f32 v10, v10, v11
	v_cvt_pk_f16_f32 v11, v12, v13
	ds_write_b64 v103, v[10:11] offset:10112
.Lepi_d4w:
	s_cmp_le_u32 s33, 1
	s_cbranch_scc1 .Lepi_v1w
	s_waitcnt vmcnt(0)
	s_cmp_le_u32 s32, 1
	s_cbranch_scc1 .Lepi_r1w
	s_cmp_eq_u32 s32, 6
	s_cbranch_scc1 .Lepi_r1w
	v_mul_f32_e32 v108, 0x3e38aa3b, v108
	v_mul_f32_e32 v109, 0x3e38aa3b, v109
	v_mul_f32_e32 v110, 0x3e38aa3b, v110
	v_mul_f32_e32 v111, 0x3e38aa3b, v111
	v_mul_f32_e32 v124, 0x3e38aa3b, v124
	v_mul_f32_e32 v125, 0x3e38aa3b, v125
	v_mul_f32_e32 v126, 0x3e38aa3b, v126
	v_mul_f32_e32 v127, 0x3e38aa3b, v127
	v_mul_f32_e32 v140, 0x3e38aa3b, v140
	v_mul_f32_e32 v141, 0x3e38aa3b, v141
	v_mul_f32_e32 v142, 0x3e38aa3b, v142
	v_mul_f32_e32 v143, 0x3e38aa3b, v143
	v_mul_f32_e32 v156, 0x3e38aa3b, v156
	v_mul_f32_e32 v157, 0x3e38aa3b, v157
	v_mul_f32_e32 v158, 0x3e38aa3b, v158
	v_mul_f32_e32 v159, 0x3e38aa3b, v159

.Lepi_d0w:
.Lepi_join:
	s_waitcnt vmcnt(0)
	s_lshl_b32 s35, s29, 11
	s_lshl_b32 s30, s5, 6
	s_sub_i32 s31, 0x80, s30
	s_sub_i32 s31, s31, s30
	v_mbcnt_lo_u32_b32 v104, -1, 0
	v_mbcnt_hi_u32_b32 v104, -1, v104
	v_lshrrev_b32_e32 v105, 3, v104
	v_and_b32_e32 v106, 7, v104
	v_mul_u32_u24_e32 v108, 0xd0, v105
	v_lshl_add_u32 v108, v106, 4, v108
	v_add_u32_e32 v108, s24, v108
	v_add_u32_e32 v108, s30, v108
	v_lshlrev_b32_e32 v109, 11, v105
	v_lshl_add_u32 v109, v106, 4, v109
	v_add_u32_e32 v102, s31, v102
	s_lshr_b32 s28, s30, 1
	s_add_i32 s28, s28, s34
	s_lshr_b32 s48, s28, 10
	s_and_b32 s28, s28, 0x3ff
	s_lshl_b32 s28, s28, 1
	s_cmp_eq_u32 s48, 1
	s_cselect_b64 s[44:45], s[16:17], s[14:15]
	s_cmp_eq_u32 s48, 2
	s_cselect_b64 s[44:45], s[18:19], s[44:45]
	s_add_u32 s44, s44, s28
	s_addc_u32 s45, s45, 0
	s_add_u32 s44, s44, s35
	s_addc_u32 s45, s45, 0
	s_lshr_b32 s28, s31, 1
	s_add_i32 s28, s28, s34
	s_lshr_b32 s48, s28, 10
	s_and_b32 s28, s28, 0x3ff
	s_lshl_b32 s28, s28, 1
	s_cmp_eq_u32 s48, 1
	s_cselect_b64 s[46:47], s[16:17], s[14:15]
	s_cmp_eq_u32 s48, 2
	s_cselect_b64 s[46:47], s[18:19], s[46:47]
	s_add_u32 s46, s46, s28
	s_addc_u32 s47, s47, 0
	s_add_u32 s46, s46, s35
	s_addc_u32 s47, s47, 0
	s_waitcnt lgkmcnt(0)
	ds_read_b128 v[2:5], v108 offset:0
	ds_read_b128 v[6:9], v108 offset:1664
	ds_read_b128 v[10:13], v108 offset:3328
	ds_read_b128 v[14:17], v108 offset:4992
	ds_read_b128 v[18:21], v108 offset:6656
	ds_read_b128 v[22:25], v108 offset:8320
	ds_read_b128 v[26:29], v108 offset:9984
	ds_read_b128 v[30:33], v108 offset:11648
	ds_read_b128 v[34:37], v102 offset:0
	ds_read_b128 v[38:41], v102 offset:3328
	ds_read_b128 v[42:45], v102 offset:6656
	ds_read_b128 v[46:49], v102 offset:9984
	v_add_u32_e32 v110, 16384, v109
	v_add_u32_e32 v111, 32768, v109
	v_add_u32_e32 v112, 49152, v109
	v_add_u32_e32 v113, 65536, v109
	v_add_u32_e32 v114, 81920, v109
	v_add_u32_e32 v115, 98304, v109
	v_add_u32_e32 v116, 114688, v109
	v_add_u32_e32 v117, 32768, v0
	v_add_u32_e32 v118, 65536, v0
	v_add_u32_e32 v119, 98304, v0
	s_waitcnt lgkmcnt(11)
	global_store_dwordx4 v109, v[2:5], s[44:45] sc1
	s_waitcnt lgkmcnt(10)
	global_store_dwordx4 v110, v[6:9], s[44:45] sc1
	s_waitcnt lgkmcnt(9)
	global_store_dwordx4 v111, v[10:13], s[44:45] sc1
	s_waitcnt lgkmcnt(8)
	global_store_dwordx4 v112, v[14:17], s[44:45] sc1
	s_waitcnt lgkmcnt(7)
	global_store_dwordx4 v113, v[18:21], s[44:45] sc1
	s_waitcnt lgkmcnt(6)
	global_store_dwordx4 v114, v[22:25], s[44:45] sc1
	s_waitcnt lgkmcnt(5)
	global_store_dwordx4 v115, v[26:29], s[44:45] sc1
	s_waitcnt lgkmcnt(4)
	global_store_dwordx4 v116, v[30:33], s[44:45] sc1
	s_waitcnt lgkmcnt(3)
	global_store_dwordx4 v0, v[34:37], s[46:47] sc1
	s_waitcnt lgkmcnt(2)
	global_store_dwordx4 v117, v[38:41], s[46:47] sc1
	s_waitcnt lgkmcnt(1)
	global_store_dwordx4 v118, v[42:45], s[46:47] sc1
	s_waitcnt lgkmcnt(0)
	global_store_dwordx4 v119, v[46:49], s[46:47] sc1
	s_branch .LBB2_2
